# speedup vs baseline: 1.0026x; 1.0026x over previous
.Ldn_loop:
	s_waitcnt lgkmcnt(0)
	v_mfma_f32_16x16x32_bf16 v[64:67], v[176:179], v[160:163], v[64:67]
	ds_read_b128 v[200:203], v11 offset:0
	v_mfma_f32_16x16x32_bf16 v[68:71], v[176:179], v[164:167], v[68:71]
	s_add_u32 m0, s20, 0x5000
	v_mfma_f32_16x16x32_bf16 v[72:75], v[176:179], v[168:171], v[72:75]
	ds_read_b128 v[204:207], v11 offset:2048
	v_mfma_f32_16x16x32_bf16 v[76:79], v[176:179], v[172:175], v[76:79]
	global_load_lds_dwordx4 v3, s[18:19]
	v_mfma_f32_16x16x32_bf16 v[80:83], v[180:183], v[160:163], v[80:83]
	ds_read_b128 v[208:211], v11 offset:4096
	v_mfma_f32_16x16x32_bf16 v[84:87], v[180:183], v[164:167], v[84:87]
	s_add_u32 m0, s20, 0x6000
	v_mfma_f32_16x16x32_bf16 v[88:91], v[180:183], v[168:171], v[88:91]
	ds_read_b128 v[212:215], v11 offset:6144
	v_mfma_f32_16x16x32_bf16 v[92:95], v[180:183], v[172:175], v[92:95]
	global_load_lds_dwordx4 v4, s[18:19]
	v_mfma_f32_16x16x32_bf16 v[96:99], v[184:187], v[160:163], v[96:99]
	ds_read_b128 v[216:219], v13 offset:0
	v_mfma_f32_16x16x32_bf16 v[100:103], v[184:187], v[164:167], v[100:103]
	s_add_u32 m0, s20, 0x7000
	v_mfma_f32_16x16x32_bf16 v[104:107], v[184:187], v[168:171], v[104:107]
	ds_read_b128 v[220:223], v13 offset:2048
	v_mfma_f32_16x16x32_bf16 v[108:111], v[184:187], v[172:175], v[108:111]
	global_load_lds_dwordx4 v5, s[18:19]
	v_mfma_f32_16x16x32_bf16 v[112:115], v[188:191], v[160:163], v[112:115]
	ds_read_b128 v[224:227], v13 offset:4096
	v_mfma_f32_16x16x32_bf16 v[116:119], v[188:191], v[164:167], v[116:119]
	s_add_u32 m0, s20, 0x8000
	v_mfma_f32_16x16x32_bf16 v[120:123], v[188:191], v[168:171], v[120:123]
	ds_read_b128 v[228:231], v13 offset:6144
	v_mfma_f32_16x16x32_bf16 v[124:127], v[188:191], v[172:175], v[124:127]
	global_load_lds_dwordx4 v6, s[18:19]
	v_mfma_f32_16x16x32_bf16 v[128:131], v[192:195], v[160:163], v[128:131]
	ds_read_b128 v[232:235], v13 offset:8192
	v_mfma_f32_16x16x32_bf16 v[132:135], v[192:195], v[164:167], v[132:135]
	s_add_u32 m0, s20, 0x9000
	v_mfma_f32_16x16x32_bf16 v[136:139], v[192:195], v[168:171], v[136:139]
	ds_read_b128 v[236:239], v13 offset:10240
	v_mfma_f32_16x16x32_bf16 v[140:143], v[192:195], v[172:175], v[140:143]
	global_load_lds_dwordx4 v7, s[18:19]
	v_mfma_f32_16x16x32_bf16 v[144:147], v[196:199], v[160:163], v[144:147]
	s_add_u32 s16, s16, 0x80
	s_addc_u32 s17, s17, 0
	s_add_u32 s18, s18, 0x80
	s_addc_u32 s19, s19, 0
	v_mfma_f32_16x16x32_bf16 v[148:151], v[196:199], v[164:167], v[148:151]
	s_add_u32 s20, s20, 0xa000
	s_sub_u32 s22, s20, 0x28000
	s_cmp_ge_u32 s20, 0x28000
	s_cselect_b32 s20, s22, s20
	v_mfma_f32_16x16x32_bf16 v[152:155], v[196:199], v[168:171], v[152:155]
	v_add_u32_e32 v10, s21, v8
	v_add_u32_e32 v12, s21, v9
	v_xor_b32_e32 v11, 64, v10
	v_xor_b32_e32 v13, 64, v12
	v_mfma_f32_16x16x32_bf16 v[156:159], v[196:199], v[172:175], v[156:159]
	s_add_u32 s21, s21, 0xa000
	s_sub_u32 s23, s21, 0x28000
	s_cmp_ge_u32 s21, 0x28000
	s_cselect_b32 s21, s23, s21
	s_waitcnt vmcnt(20) lgkmcnt(0)
	s_barrier
	v_mfma_f32_16x16x32_bf16 v[64:67], v[216:219], v[200:203], v[64:67]
	ds_read_b128 v[160:163], v10 offset:0
	v_mfma_f32_16x16x32_bf16 v[68:71], v[216:219], v[204:207], v[68:71]
	s_add_u32 m0, s20, 0x0
	v_mfma_f32_16x16x32_bf16 v[72:75], v[216:219], v[208:211], v[72:75]
	ds_read_b128 v[164:167], v10 offset:2048
	v_mfma_f32_16x16x32_bf16 v[76:79], v[216:219], v[212:215], v[76:79]
	global_load_lds_dwordx4 v2, s[16:17]
	v_mfma_f32_16x16x32_bf16 v[80:83], v[220:223], v[200:203], v[80:83]
	ds_read_b128 v[168:171], v10 offset:4096
	v_mfma_f32_16x16x32_bf16 v[84:87], v[220:223], v[204:207], v[84:87]
	s_add_u32 m0, s20, 0x1000
	v_mfma_f32_16x16x32_bf16 v[88:91], v[220:223], v[208:211], v[88:91]
	ds_read_b128 v[172:175], v10 offset:6144
	v_mfma_f32_16x16x32_bf16 v[92:95], v[220:223], v[212:215], v[92:95]
	global_load_lds_dwordx4 v3, s[16:17]
	v_mfma_f32_16x16x32_bf16 v[96:99], v[224:227], v[200:203], v[96:99]
	ds_read_b128 v[176:179], v12 offset:0
	v_mfma_f32_16x16x32_bf16 v[100:103], v[224:227], v[204:207], v[100:103]
	s_add_u32 m0, s20, 0x2000
	v_mfma_f32_16x16x32_bf16 v[104:107], v[224:227], v[208:211], v[104:107]
	ds_read_b128 v[180:183], v12 offset:2048
	v_mfma_f32_16x16x32_bf16 v[108:111], v[224:227], v[212:215], v[108:111]
	global_load_lds_dwordx4 v4, s[16:17]
	v_mfma_f32_16x16x32_bf16 v[112:115], v[228:231], v[200:203], v[112:115]
	ds_read_b128 v[184:187], v12 offset:4096
	v_mfma_f32_16x16x32_bf16 v[116:119], v[228:231], v[204:207], v[116:119]
	s_add_u32 m0, s20, 0x3000
	v_mfma_f32_16x16x32_bf16 v[120:123], v[228:231], v[208:211], v[120:123]
	ds_read_b128 v[188:191], v12 offset:6144
	v_mfma_f32_16x16x32_bf16 v[124:127], v[228:231], v[212:215], v[124:127]
	global_load_lds_dwordx4 v5, s[16:17]
	v_mfma_f32_16x16x32_bf16 v[128:131], v[232:235], v[200:203], v[128:131]
	ds_read_b128 v[192:195], v12 offset:8192
	v_mfma_f32_16x16x32_bf16 v[132:135], v[232:235], v[204:207], v[132:135]
	s_add_u32 m0, s20, 0x4000
	v_mfma_f32_16x16x32_bf16 v[136:139], v[232:235], v[208:211], v[136:139]
	ds_read_b128 v[196:199], v12 offset:10240
	v_mfma_f32_16x16x32_bf16 v[140:143], v[232:235], v[212:215], v[140:143]
	global_load_lds_dwordx4 v2, s[18:19]
	v_mfma_f32_16x16x32_bf16 v[144:147], v[236:239], v[200:203], v[144:147]
	v_mfma_f32_16x16x32_bf16 v[148:151], v[236:239], v[204:207], v[148:151]
	v_mfma_f32_16x16x32_bf16 v[152:155], v[236:239], v[208:211], v[152:155]
	v_mfma_f32_16x16x32_bf16 v[156:159], v[236:239], v[212:215], v[156:159]
	s_add_u32 s15, s15, 1
	s_cmp_lt_u32 s15, 44
	s_cbranch_scc1 .Ldn_loop
	s_waitcnt lgkmcnt(0)
	v_mfma_f32_16x16x32_bf16 v[64:67], v[176:179], v[160:163], v[64:67]
	ds_read_b128 v[200:203], v11 offset:0
	v_mfma_f32_16x16x32_bf16 v[68:71], v[176:179], v[164:167], v[68:71]
	s_add_u32 m0, s20, 0x5000
	v_mfma_f32_16x16x32_bf16 v[72:75], v[176:179], v[168:171], v[72:75]
	ds_read_b128 v[204:207], v11 offset:2048
	v_mfma_f32_16x16x32_bf16 v[76:79], v[176:179], v[172:175], v[76:79]
	global_load_lds_dwordx4 v3, s[18:19]
	v_mfma_f32_16x16x32_bf16 v[80:83], v[180:183], v[160:163], v[80:83]
	ds_read_b128 v[208:211], v11 offset:4096
	v_mfma_f32_16x16x32_bf16 v[84:87], v[180:183], v[164:167], v[84:87]
	s_add_u32 m0, s20, 0x6000
	v_mfma_f32_16x16x32_bf16 v[88:91], v[180:183], v[168:171], v[88:91]
	ds_read_b128 v[212:215], v11 offset:6144
	v_mfma_f32_16x16x32_bf16 v[92:95], v[180:183], v[172:175], v[92:95]
	global_load_lds_dwordx4 v4, s[18:19]
	v_mfma_f32_16x16x32_bf16 v[96:99], v[184:187], v[160:163], v[96:99]
	ds_read_b128 v[216:219], v13 offset:0
	v_mfma_f32_16x16x32_bf16 v[100:103], v[184:187], v[164:167], v[100:103]
	s_add_u32 m0, s20, 0x7000
	v_mfma_f32_16x16x32_bf16 v[104:107], v[184:187], v[168:171], v[104:107]
	ds_read_b128 v[220:223], v13 offset:2048
	v_mfma_f32_16x16x32_bf16 v[108:111], v[184:187], v[172:175], v[108:111]
	global_load_lds_dwordx4 v5, s[18:19]
	v_mfma_f32_16x16x32_bf16 v[112:115], v[188:191], v[160:163], v[112:115]
	ds_read_b128 v[224:227], v13 offset:4096
	v_mfma_f32_16x16x32_bf16 v[116:119], v[188:191], v[164:167], v[116:119]
	s_add_u32 m0, s20, 0x8000
	v_mfma_f32_16x16x32_bf16 v[120:123], v[188:191], v[168:171], v[120:123]
	ds_read_b128 v[228:231], v13 offset:6144
	v_mfma_f32_16x16x32_bf16 v[124:127], v[188:191], v[172:175], v[124:127]
	global_load_lds_dwordx4 v6, s[18:19]
	v_mfma_f32_16x16x32_bf16 v[128:131], v[192:195], v[160:163], v[128:131]
	ds_read_b128 v[232:235], v13 offset:8192
	v_mfma_f32_16x16x32_bf16 v[132:135], v[192:195], v[164:167], v[132:135]
	s_add_u32 m0, s20, 0x9000
	v_mfma_f32_16x16x32_bf16 v[136:139], v[192:195], v[168:171], v[136:139]
	ds_read_b128 v[236:239], v13 offset:10240
	v_mfma_f32_16x16x32_bf16 v[140:143], v[192:195], v[172:175], v[140:143]
	global_load_lds_dwordx4 v7, s[18:19]
	v_mfma_f32_16x16x32_bf16 v[144:147], v[196:199], v[160:163], v[144:147]
	s_add_u32 s16, s16, 0x80
	s_addc_u32 s17, s17, 0
	s_add_u32 s18, s18, 0x80
	s_addc_u32 s19, s19, 0
	v_mfma_f32_16x16x32_bf16 v[148:151], v[196:199], v[164:167], v[148:151]
	s_add_u32 s20, s20, 0xa000
	s_sub_u32 s22, s20, 0x28000
	s_cmp_ge_u32 s20, 0x28000
	s_cselect_b32 s20, s22, s20
	v_mfma_f32_16x16x32_bf16 v[152:155], v[196:199], v[168:171], v[152:155]
	v_add_u32_e32 v10, s21, v8
	v_add_u32_e32 v12, s21, v9
	v_xor_b32_e32 v11, 64, v10
	v_xor_b32_e32 v13, 64, v12
	v_mfma_f32_16x16x32_bf16 v[156:159], v[196:199], v[172:175], v[156:159]
	s_add_u32 s21, s21, 0xa000
	s_sub_u32 s23, s21, 0x28000
	s_cmp_ge_u32 s21, 0x28000
	s_cselect_b32 s21, s23, s21
	s_waitcnt vmcnt(20) lgkmcnt(0)
	s_barrier
	v_mfma_f32_16x16x32_bf16 v[64:67], v[216:219], v[200:203], v[64:67]
	ds_read_b128 v[160:163], v10 offset:0
	v_mfma_f32_16x16x32_bf16 v[68:71], v[216:219], v[204:207], v[68:71]
	ds_read_b128 v[164:167], v10 offset:2048
	v_mfma_f32_16x16x32_bf16 v[72:75], v[216:219], v[208:211], v[72:75]
	ds_read_b128 v[168:171], v10 offset:4096
	v_mfma_f32_16x16x32_bf16 v[76:79], v[216:219], v[212:215], v[76:79]
	ds_read_b128 v[172:175], v10 offset:6144
	v_mfma_f32_16x16x32_bf16 v[80:83], v[220:223], v[200:203], v[80:83]
	ds_read_b128 v[176:179], v12 offset:0
	v_mfma_f32_16x16x32_bf16 v[84:87], v[220:223], v[204:207], v[84:87]
	ds_read_b128 v[180:183], v12 offset:2048
	v_mfma_f32_16x16x32_bf16 v[88:91], v[220:223], v[208:211], v[88:91]
	ds_read_b128 v[184:187], v12 offset:4096
	v_mfma_f32_16x16x32_bf16 v[92:95], v[220:223], v[212:215], v[92:95]
	ds_read_b128 v[188:191], v12 offset:6144
	v_mfma_f32_16x16x32_bf16 v[96:99], v[224:227], v[200:203], v[96:99]
	ds_read_b128 v[192:195], v12 offset:8192
	v_mfma_f32_16x16x32_bf16 v[100:103], v[224:227], v[204:207], v[100:103]
	ds_read_b128 v[196:199], v12 offset:10240
	v_mfma_f32_16x16x32_bf16 v[104:107], v[224:227], v[208:211], v[104:107]
	v_mfma_f32_16x16x32_bf16 v[108:111], v[224:227], v[212:215], v[108:111]
	v_mfma_f32_16x16x32_bf16 v[112:115], v[228:231], v[200:203], v[112:115]
	v_mfma_f32_16x16x32_bf16 v[116:119], v[228:231], v[204:207], v[116:119]
	v_mfma_f32_16x16x32_bf16 v[120:123], v[228:231], v[208:211], v[120:123]
	v_mfma_f32_16x16x32_bf16 v[124:127], v[228:231], v[212:215], v[124:127]
	v_mfma_f32_16x16x32_bf16 v[128:131], v[232:235], v[200:203], v[128:131]
	v_mfma_f32_16x16x32_bf16 v[132:135], v[232:235], v[204:207], v[132:135]
	v_mfma_f32_16x16x32_bf16 v[136:139], v[232:235], v[208:211], v[136:139]
	v_mfma_f32_16x16x32_bf16 v[140:143], v[232:235], v[212:215], v[140:143]
	v_mfma_f32_16x16x32_bf16 v[144:147], v[236:239], v[200:203], v[144:147]
	v_mfma_f32_16x16x32_bf16 v[148:151], v[236:239], v[204:207], v[148:151]
	v_mfma_f32_16x16x32_bf16 v[152:155], v[236:239], v[208:211], v[152:155]
	v_mfma_f32_16x16x32_bf16 v[156:159], v[236:239], v[212:215], v[156:159]
	s_waitcnt lgkmcnt(0)
	v_mfma_f32_16x16x32_bf16 v[64:67], v[176:179], v[160:163], v[64:67]
	ds_read_b128 v[200:203], v11 offset:0
	v_mfma_f32_16x16x32_bf16 v[68:71], v[176:179], v[164:167], v[68:71]
	ds_read_b128 v[204:207], v11 offset:2048
	v_mfma_f32_16x16x32_bf16 v[72:75], v[176:179], v[168:171], v[72:75]
	ds_read_b128 v[208:211], v11 offset:4096
	v_mfma_f32_16x16x32_bf16 v[76:79], v[176:179], v[172:175], v[76:79]
	ds_read_b128 v[212:215], v11 offset:6144
	v_mfma_f32_16x16x32_bf16 v[80:83], v[180:183], v[160:163], v[80:83]
	ds_read_b128 v[216:219], v13 offset:0
	v_mfma_f32_16x16x32_bf16 v[84:87], v[180:183], v[164:167], v[84:87]
	ds_read_b128 v[220:223], v13 offset:2048
	v_mfma_f32_16x16x32_bf16 v[88:91], v[180:183], v[168:171], v[88:91]
	ds_read_b128 v[224:227], v13 offset:4096
	v_mfma_f32_16x16x32_bf16 v[92:95], v[180:183], v[172:175], v[92:95]
	ds_read_b128 v[228:231], v13 offset:6144
	v_mfma_f32_16x16x32_bf16 v[96:99], v[184:187], v[160:163], v[96:99]
	ds_read_b128 v[232:235], v13 offset:8192
	v_mfma_f32_16x16x32_bf16 v[100:103], v[184:187], v[164:167], v[100:103]
	ds_read_b128 v[236:239], v13 offset:10240
	v_mfma_f32_16x16x32_bf16 v[104:107], v[184:187], v[168:171], v[104:107]
	v_mfma_f32_16x16x32_bf16 v[108:111], v[184:187], v[172:175], v[108:111]
	v_mfma_f32_16x16x32_bf16 v[112:115], v[188:191], v[160:163], v[112:115]
	v_mfma_f32_16x16x32_bf16 v[116:119], v[188:191], v[164:167], v[116:119]
	v_mfma_f32_16x16x32_bf16 v[120:123], v[188:191], v[168:171], v[120:123]
	v_mfma_f32_16x16x32_bf16 v[124:127], v[188:191], v[172:175], v[124:127]
	v_mfma_f32_16x16x32_bf16 v[128:131], v[192:195], v[160:163], v[128:131]
	v_mfma_f32_16x16x32_bf16 v[132:135], v[192:195], v[164:167], v[132:135]
	v_mfma_f32_16x16x32_bf16 v[136:139], v[192:195], v[168:171], v[136:139]
	v_mfma_f32_16x16x32_bf16 v[140:143], v[192:195], v[172:175], v[140:143]
	v_mfma_f32_16x16x32_bf16 v[144:147], v[196:199], v[160:163], v[144:147]
	v_add_u32_e32 v10, s21, v8
	v_add_u32_e32 v12, s21, v9
	v_xor_b32_e32 v11, 64, v10
	v_xor_b32_e32 v13, 64, v12
	v_mfma_f32_16x16x32_bf16 v[148:151], v[196:199], v[164:167], v[148:151]
	s_add_u32 s21, s21, 0xa000
	s_sub_u32 s23, s21, 0x28000
	s_cmp_ge_u32 s21, 0x28000
	s_cselect_b32 s21, s23, s21
	v_mfma_f32_16x16x32_bf16 v[152:155], v[196:199], v[168:171], v[152:155]
	v_mfma_f32_16x16x32_bf16 v[156:159], v[196:199], v[172:175], v[156:159]
	s_waitcnt vmcnt(10) lgkmcnt(0)
	s_barrier
	v_mfma_f32_16x16x32_bf16 v[64:67], v[216:219], v[200:203], v[64:67]
	ds_read_b128 v[160:163], v10 offset:0
	v_mfma_f32_16x16x32_bf16 v[68:71], v[216:219], v[204:207], v[68:71]
	ds_read_b128 v[164:167], v10 offset:2048
	v_mfma_f32_16x16x32_bf16 v[72:75], v[216:219], v[208:211], v[72:75]
	ds_read_b128 v[168:171], v10 offset:4096
	v_mfma_f32_16x16x32_bf16 v[76:79], v[216:219], v[212:215], v[76:79]
	ds_read_b128 v[172:175], v10 offset:6144
	v_mfma_f32_16x16x32_bf16 v[80:83], v[220:223], v[200:203], v[80:83]
	ds_read_b128 v[176:179], v12 offset:0
	v_mfma_f32_16x16x32_bf16 v[84:87], v[220:223], v[204:207], v[84:87]
	ds_read_b128 v[180:183], v12 offset:2048
	v_mfma_f32_16x16x32_bf16 v[88:91], v[220:223], v[208:211], v[88:91]
	ds_read_b128 v[184:187], v12 offset:4096
	v_mfma_f32_16x16x32_bf16 v[92:95], v[220:223], v[212:215], v[92:95]
	ds_read_b128 v[188:191], v12 offset:6144
	v_mfma_f32_16x16x32_bf16 v[96:99], v[224:227], v[200:203], v[96:99]
	ds_read_b128 v[192:195], v12 offset:8192
	v_mfma_f32_16x16x32_bf16 v[100:103], v[224:227], v[204:207], v[100:103]
	ds_read_b128 v[196:199], v12 offset:10240
	v_mfma_f32_16x16x32_bf16 v[104:107], v[224:227], v[208:211], v[104:107]
	v_mfma_f32_16x16x32_bf16 v[108:111], v[224:227], v[212:215], v[108:111]
	v_mfma_f32_16x16x32_bf16 v[112:115], v[228:231], v[200:203], v[112:115]
	v_mfma_f32_16x16x32_bf16 v[116:119], v[228:231], v[204:207], v[116:119]
	v_mfma_f32_16x16x32_bf16 v[120:123], v[228:231], v[208:211], v[120:123]
	v_mfma_f32_16x16x32_bf16 v[124:127], v[228:231], v[212:215], v[124:127]
	v_mfma_f32_16x16x32_bf16 v[128:131], v[232:235], v[200:203], v[128:131]
	v_mfma_f32_16x16x32_bf16 v[132:135], v[232:235], v[204:207], v[132:135]
	v_mfma_f32_16x16x32_bf16 v[136:139], v[232:235], v[208:211], v[136:139]
	v_mfma_f32_16x16x32_bf16 v[140:143], v[232:235], v[212:215], v[140:143]
	v_mfma_f32_16x16x32_bf16 v[144:147], v[236:239], v[200:203], v[144:147]
	v_mfma_f32_16x16x32_bf16 v[148:151], v[236:239], v[204:207], v[148:151]
	v_mfma_f32_16x16x32_bf16 v[152:155], v[236:239], v[208:211], v[152:155]
	v_mfma_f32_16x16x32_bf16 v[156:159], v[236:239], v[212:215], v[156:159]
	s_waitcnt lgkmcnt(0)
	v_mfma_f32_16x16x32_bf16 v[64:67], v[176:179], v[160:163], v[64:67]
	ds_read_b128 v[200:203], v11 offset:0
	v_mfma_f32_16x16x32_bf16 v[68:71], v[176:179], v[164:167], v[68:71]
	ds_read_b128 v[204:207], v11 offset:2048
	v_mfma_f32_16x16x32_bf16 v[72:75], v[176:179], v[168:171], v[72:75]
	ds_read_b128 v[208:211], v11 offset:4096
	v_mfma_f32_16x16x32_bf16 v[76:79], v[176:179], v[172:175], v[76:79]
	ds_read_b128 v[212:215], v11 offset:6144
	v_mfma_f32_16x16x32_bf16 v[80:83], v[180:183], v[160:163], v[80:83]
	ds_read_b128 v[216:219], v13 offset:0
	v_mfma_f32_16x16x32_bf16 v[84:87], v[180:183], v[164:167], v[84:87]
	ds_read_b128 v[220:223], v13 offset:2048
	v_mfma_f32_16x16x32_bf16 v[88:91], v[180:183], v[168:171], v[88:91]
	ds_read_b128 v[224:227], v13 offset:4096
	v_mfma_f32_16x16x32_bf16 v[92:95], v[180:183], v[172:175], v[92:95]
	ds_read_b128 v[228:231], v13 offset:6144
	v_mfma_f32_16x16x32_bf16 v[96:99], v[184:187], v[160:163], v[96:99]
	ds_read_b128 v[232:235], v13 offset:8192
	v_mfma_f32_16x16x32_bf16 v[100:103], v[184:187], v[164:167], v[100:103]
	ds_read_b128 v[236:239], v13 offset:10240
	v_mfma_f32_16x16x32_bf16 v[104:107], v[184:187], v[168:171], v[104:107]
	v_mfma_f32_16x16x32_bf16 v[108:111], v[184:187], v[172:175], v[108:111]
	v_mfma_f32_16x16x32_bf16 v[112:115], v[188:191], v[160:163], v[112:115]
	v_mfma_f32_16x16x32_bf16 v[116:119], v[188:191], v[164:167], v[116:119]
	v_mfma_f32_16x16x32_bf16 v[120:123], v[188:191], v[168:171], v[120:123]
	v_mfma_f32_16x16x32_bf16 v[124:127], v[188:191], v[172:175], v[124:127]
	v_mfma_f32_16x16x32_bf16 v[128:131], v[192:195], v[160:163], v[128:131]
	v_mfma_f32_16x16x32_bf16 v[132:135], v[192:195], v[164:167], v[132:135]
	v_mfma_f32_16x16x32_bf16 v[136:139], v[192:195], v[168:171], v[136:139]
	v_mfma_f32_16x16x32_bf16 v[140:143], v[192:195], v[172:175], v[140:143]
	v_mfma_f32_16x16x32_bf16 v[144:147], v[196:199], v[160:163], v[144:147]
	v_add_u32_e32 v10, s21, v8
	v_add_u32_e32 v12, s21, v9
	v_xor_b32_e32 v11, 64, v10
	v_xor_b32_e32 v13, 64, v12
	v_mfma_f32_16x16x32_bf16 v[148:151], v[196:199], v[164:167], v[148:151]
	s_add_u32 s21, s21, 0xa000
	s_sub_u32 s23, s21, 0x28000
	s_cmp_ge_u32 s21, 0x28000
	s_cselect_b32 s21, s23, s21
	v_mfma_f32_16x16x32_bf16 v[152:155], v[196:199], v[168:171], v[152:155]
	v_mfma_f32_16x16x32_bf16 v[156:159], v[196:199], v[172:175], v[156:159]
	s_waitcnt vmcnt(0) lgkmcnt(0)
	s_barrier
	v_mfma_f32_16x16x32_bf16 v[64:67], v[216:219], v[200:203], v[64:67]
	ds_read_b128 v[160:163], v10 offset:0
	v_mfma_f32_16x16x32_bf16 v[68:71], v[216:219], v[204:207], v[68:71]
	global_load_dwordx4 v[16:19], v56, s[8:9] offset:0
	v_mfma_f32_16x16x32_bf16 v[72:75], v[216:219], v[208:211], v[72:75]
	ds_read_b128 v[164:167], v10 offset:2048
	v_mfma_f32_16x16x32_bf16 v[76:79], v[216:219], v[212:215], v[76:79]
	global_load_dwordx4 v[20:23], v57, s[8:9] offset:0
	v_mfma_f32_16x16x32_bf16 v[80:83], v[220:223], v[200:203], v[80:83]
	ds_read_b128 v[168:171], v10 offset:4096
	v_mfma_f32_16x16x32_bf16 v[84:87], v[220:223], v[204:207], v[84:87]
	global_load_dwordx4 v[24:27], v58, s[8:9] offset:0
	v_mfma_f32_16x16x32_bf16 v[88:91], v[220:223], v[208:211], v[88:91]
	ds_read_b128 v[172:175], v10 offset:6144
	v_mfma_f32_16x16x32_bf16 v[92:95], v[220:223], v[212:215], v[92:95]
	global_load_dwordx4 v[28:31], v59, s[8:9] offset:0
	v_mfma_f32_16x16x32_bf16 v[96:99], v[224:227], v[200:203], v[96:99]
	ds_read_b128 v[176:179], v12 offset:0
	v_mfma_f32_16x16x32_bf16 v[100:103], v[224:227], v[204:207], v[100:103]
	global_load_dwordx4 v[32:35], v56, s[8:9] offset:64
	v_mfma_f32_16x16x32_bf16 v[104:107], v[224:227], v[208:211], v[104:107]
	ds_read_b128 v[180:183], v12 offset:2048
	v_mfma_f32_16x16x32_bf16 v[108:111], v[224:227], v[212:215], v[108:111]
	global_load_dwordx4 v[36:39], v57, s[8:9] offset:64
	v_mfma_f32_16x16x32_bf16 v[112:115], v[228:231], v[200:203], v[112:115]
	ds_read_b128 v[184:187], v12 offset:4096
	v_mfma_f32_16x16x32_bf16 v[116:119], v[228:231], v[204:207], v[116:119]
	global_load_dwordx4 v[40:43], v58, s[8:9] offset:64
	v_mfma_f32_16x16x32_bf16 v[120:123], v[228:231], v[208:211], v[120:123]
	ds_read_b128 v[188:191], v12 offset:6144
	v_mfma_f32_16x16x32_bf16 v[124:127], v[228:231], v[212:215], v[124:127]
	global_load_dwordx4 v[44:47], v59, s[8:9] offset:64
	v_mfma_f32_16x16x32_bf16 v[128:131], v[232:235], v[200:203], v[128:131]
	ds_read_b128 v[192:195], v12 offset:8192
	v_mfma_f32_16x16x32_bf16 v[132:135], v[232:235], v[204:207], v[132:135]
	global_load_dwordx4 v[48:51], v56, s[8:9] offset:128
	v_mfma_f32_16x16x32_bf16 v[136:139], v[232:235], v[208:211], v[136:139]
	ds_read_b128 v[196:199], v12 offset:10240
	v_mfma_f32_16x16x32_bf16 v[140:143], v[232:235], v[212:215], v[140:143]
	global_load_dwordx4 v[52:55], v57, s[8:9] offset:128
	v_mfma_f32_16x16x32_bf16 v[144:147], v[236:239], v[200:203], v[144:147]
	global_load_dwordx4 v[240:243], v58, s[8:9] offset:128
	v_mfma_f32_16x16x32_bf16 v[148:151], v[236:239], v[204:207], v[148:151]
	global_load_dwordx4 v[244:247], v59, s[8:9] offset:128
	v_mfma_f32_16x16x32_bf16 v[152:155], v[236:239], v[208:211], v[152:155]
	global_load_dwordx4 v[248:251], v56, s[8:9] offset:192
	v_mfma_f32_16x16x32_bf16 v[156:159], v[236:239], v[212:215], v[156:159]
	global_load_dwordx4 v[252:255], v57, s[8:9] offset:192
	s_waitcnt lgkmcnt(0)
	v_mfma_f32_16x16x32_bf16 v[64:67], v[176:179], v[160:163], v[64:67]
	ds_read_b128 v[200:203], v11 offset:0
	v_mfma_f32_16x16x32_bf16 v[68:71], v[176:179], v[164:167], v[68:71]
	ds_read_b128 v[204:207], v11 offset:2048
	v_mfma_f32_16x16x32_bf16 v[72:75], v[176:179], v[168:171], v[72:75]
	ds_read_b128 v[208:211], v11 offset:4096
	v_mfma_f32_16x16x32_bf16 v[76:79], v[176:179], v[172:175], v[76:79]
	ds_read_b128 v[212:215], v11 offset:6144
	v_mfma_f32_16x16x32_bf16 v[80:83], v[180:183], v[160:163], v[80:83]
	ds_read_b128 v[216:219], v13 offset:0
	v_mfma_f32_16x16x32_bf16 v[84:87], v[180:183], v[164:167], v[84:87]
	ds_read_b128 v[220:223], v13 offset:2048
	v_mfma_f32_16x16x32_bf16 v[88:91], v[180:183], v[168:171], v[88:91]
	ds_read_b128 v[224:227], v13 offset:4096
	v_mfma_f32_16x16x32_bf16 v[92:95], v[180:183], v[172:175], v[92:95]
	ds_read_b128 v[228:231], v13 offset:6144
	v_mfma_f32_16x16x32_bf16 v[96:99], v[184:187], v[160:163], v[96:99]
	ds_read_b128 v[232:235], v13 offset:8192
	v_mfma_f32_16x16x32_bf16 v[100:103], v[184:187], v[164:167], v[100:103]
	ds_read_b128 v[236:239], v13 offset:10240
	v_mfma_f32_16x16x32_bf16 v[104:107], v[184:187], v[168:171], v[104:107]
	v_mfma_f32_16x16x32_bf16 v[108:111], v[184:187], v[172:175], v[108:111]
	v_mfma_f32_16x16x32_bf16 v[112:115], v[188:191], v[160:163], v[112:115]
	v_mfma_f32_16x16x32_bf16 v[116:119], v[188:191], v[164:167], v[116:119]
	v_mfma_f32_16x16x32_bf16 v[120:123], v[188:191], v[168:171], v[120:123]
	v_mfma_f32_16x16x32_bf16 v[124:127], v[188:191], v[172:175], v[124:127]
	v_mfma_f32_16x16x32_bf16 v[128:131], v[192:195], v[160:163], v[128:131]
	v_mfma_f32_16x16x32_bf16 v[132:135], v[192:195], v[164:167], v[132:135]
	v_mfma_f32_16x16x32_bf16 v[136:139], v[192:195], v[168:171], v[136:139]
	v_mfma_f32_16x16x32_bf16 v[140:143], v[192:195], v[172:175], v[140:143]
	v_mfma_f32_16x16x32_bf16 v[144:147], v[196:199], v[160:163], v[144:147]
	v_mfma_f32_16x16x32_bf16 v[148:151], v[196:199], v[164:167], v[148:151]
	v_mfma_f32_16x16x32_bf16 v[152:155], v[196:199], v[168:171], v[152:155]
	v_mfma_f32_16x16x32_bf16 v[156:159], v[196:199], v[172:175], v[156:159]
	s_waitcnt lgkmcnt(0)
	v_mfma_f32_16x16x32_bf16 v[64:67], v[216:219], v[200:203], v[64:67]
	v_mfma_f32_16x16x32_bf16 v[68:71], v[216:219], v[204:207], v[68:71]
	global_load_dwordx4 v[160:163], v58, s[8:9] offset:192
	v_mfma_f32_16x16x32_bf16 v[72:75], v[216:219], v[208:211], v[72:75]
	v_mfma_f32_16x16x32_bf16 v[76:79], v[216:219], v[212:215], v[76:79]
	global_load_dwordx4 v[164:167], v59, s[8:9] offset:192
	v_mfma_f32_16x16x32_bf16 v[80:83], v[220:223], v[200:203], v[80:83]
	v_mfma_f32_16x16x32_bf16 v[84:87], v[220:223], v[204:207], v[84:87]
	global_load_dwordx4 v[168:171], v56, s[8:9] offset:256
	v_mfma_f32_16x16x32_bf16 v[88:91], v[220:223], v[208:211], v[88:91]
	v_mfma_f32_16x16x32_bf16 v[92:95], v[220:223], v[212:215], v[92:95]
	global_load_dwordx4 v[172:175], v57, s[8:9] offset:256
	v_mfma_f32_16x16x32_bf16 v[96:99], v[224:227], v[200:203], v[96:99]
	v_mfma_f32_16x16x32_bf16 v[100:103], v[224:227], v[204:207], v[100:103]
	global_load_dwordx4 v[176:179], v58, s[8:9] offset:256
	v_mfma_f32_16x16x32_bf16 v[104:107], v[224:227], v[208:211], v[104:107]
	v_mfma_f32_16x16x32_bf16 v[108:111], v[224:227], v[212:215], v[108:111]
	global_load_dwordx4 v[180:183], v59, s[8:9] offset:256
	v_mfma_f32_16x16x32_bf16 v[112:115], v[228:231], v[200:203], v[112:115]
	v_mfma_f32_16x16x32_bf16 v[116:119], v[228:231], v[204:207], v[116:119]
	global_load_dwordx4 v[184:187], v56, s[8:9] offset:320
	v_mfma_f32_16x16x32_bf16 v[120:123], v[228:231], v[208:211], v[120:123]
	v_mfma_f32_16x16x32_bf16 v[124:127], v[228:231], v[212:215], v[124:127]
	global_load_dwordx4 v[188:191], v57, s[8:9] offset:320
	v_mfma_f32_16x16x32_bf16 v[128:131], v[232:235], v[200:203], v[128:131]
	v_mfma_f32_16x16x32_bf16 v[132:135], v[232:235], v[204:207], v[132:135]
	global_load_dwordx4 v[192:195], v58, s[8:9] offset:320
	v_mfma_f32_16x16x32_bf16 v[136:139], v[232:235], v[208:211], v[136:139]
	v_mfma_f32_16x16x32_bf16 v[140:143], v[232:235], v[212:215], v[140:143]
	global_load_dwordx4 v[196:199], v59, s[8:9] offset:320
	v_mfma_f32_16x16x32_bf16 v[144:147], v[236:239], v[200:203], v[144:147]
	v_mfma_f32_16x16x32_bf16 v[148:151], v[236:239], v[204:207], v[148:151]
	v_mfma_f32_16x16x32_bf16 v[152:155], v[236:239], v[208:211], v[152:155]
	v_mfma_f32_16x16x32_bf16 v[156:159], v[236:239], v[212:215], v[156:159]
	s_waitcnt vmcnt(23)
	v_pk_add_f32 v[64:65], v[64:65], v[16:17]
	v_pk_add_f32 v[66:67], v[66:67], v[18:19]
	global_store_dwordx4 v56, v[64:67], s[10:11] offset:0 sc0 sc1
	s_waitcnt vmcnt(23)
	v_pk_add_f32 v[68:69], v[68:69], v[20:21]
	v_pk_add_f32 v[70:71], v[70:71], v[22:23]
	global_store_dwordx4 v57, v[68:71], s[10:11] offset:0 sc0 sc1
	s_waitcnt vmcnt(23)
	v_pk_add_f32 v[72:73], v[72:73], v[24:25]
	v_pk_add_f32 v[74:75], v[74:75], v[26:27]
	global_store_dwordx4 v58, v[72:75], s[10:11] offset:0 sc0 sc1
	s_waitcnt vmcnt(23)
	v_pk_add_f32 v[76:77], v[76:77], v[28:29]
	v_pk_add_f32 v[78:79], v[78:79], v[30:31]
	global_store_dwordx4 v59, v[76:79], s[10:11] offset:0 sc0 sc1
	s_waitcnt vmcnt(23)
	v_pk_add_f32 v[80:81], v[80:81], v[32:33]
	v_pk_add_f32 v[82:83], v[82:83], v[34:35]
	global_store_dwordx4 v56, v[80:83], s[10:11] offset:64 sc0 sc1
	s_waitcnt vmcnt(23)
	v_pk_add_f32 v[84:85], v[84:85], v[36:37]
	v_pk_add_f32 v[86:87], v[86:87], v[38:39]
	global_store_dwordx4 v57, v[84:87], s[10:11] offset:64 sc0 sc1
	s_waitcnt vmcnt(23)
	v_pk_add_f32 v[88:89], v[88:89], v[40:41]
	v_pk_add_f32 v[90:91], v[90:91], v[42:43]
	global_store_dwordx4 v58, v[88:91], s[10:11] offset:64 sc0 sc1
	s_waitcnt vmcnt(23)
	v_pk_add_f32 v[92:93], v[92:93], v[44:45]
	v_pk_add_f32 v[94:95], v[94:95], v[46:47]
	global_store_dwordx4 v59, v[92:95], s[10:11] offset:64 sc0 sc1
	s_waitcnt vmcnt(23)
	v_pk_add_f32 v[96:97], v[96:97], v[48:49]
	v_pk_add_f32 v[98:99], v[98:99], v[50:51]
	global_store_dwordx4 v56, v[96:99], s[10:11] offset:128 sc0 sc1
	s_waitcnt vmcnt(23)
	v_pk_add_f32 v[100:101], v[100:101], v[52:53]
	v_pk_add_f32 v[102:103], v[102:103], v[54:55]
	global_store_dwordx4 v57, v[100:103], s[10:11] offset:128 sc0 sc1
	s_waitcnt vmcnt(23)
	v_pk_add_f32 v[104:105], v[104:105], v[240:241]
	v_pk_add_f32 v[106:107], v[106:107], v[242:243]
	global_store_dwordx4 v58, v[104:107], s[10:11] offset:128 sc0 sc1
	s_waitcnt vmcnt(23)
	v_pk_add_f32 v[108:109], v[108:109], v[244:245]
	v_pk_add_f32 v[110:111], v[110:111], v[246:247]
	global_store_dwordx4 v59, v[108:111], s[10:11] offset:128 sc0 sc1
	s_waitcnt vmcnt(23)
	v_pk_add_f32 v[112:113], v[112:113], v[248:249]
	v_pk_add_f32 v[114:115], v[114:115], v[250:251]
	global_store_dwordx4 v56, v[112:115], s[10:11] offset:192 sc0 sc1
	s_waitcnt vmcnt(23)
	v_pk_add_f32 v[116:117], v[116:117], v[252:253]
	v_pk_add_f32 v[118:119], v[118:119], v[254:255]
	global_store_dwordx4 v57, v[116:119], s[10:11] offset:192 sc0 sc1
	s_waitcnt vmcnt(23)
	v_pk_add_f32 v[120:121], v[120:121], v[160:161]
	v_pk_add_f32 v[122:123], v[122:123], v[162:163]
	global_store_dwordx4 v58, v[120:123], s[10:11] offset:192 sc0 sc1
	s_waitcnt vmcnt(23)
	v_pk_add_f32 v[124:125], v[124:125], v[164:165]
	v_pk_add_f32 v[126:127], v[126:127], v[166:167]
	global_store_dwordx4 v59, v[124:127], s[10:11] offset:192 sc0 sc1
	s_waitcnt vmcnt(23)
	v_pk_add_f32 v[128:129], v[128:129], v[168:169]
	v_pk_add_f32 v[130:131], v[130:131], v[170:171]
	global_store_dwordx4 v56, v[128:131], s[10:11] offset:256 sc0 sc1
	s_waitcnt vmcnt(23)
	v_pk_add_f32 v[132:133], v[132:133], v[172:173]
	v_pk_add_f32 v[134:135], v[134:135], v[174:175]
	global_store_dwordx4 v57, v[132:135], s[10:11] offset:256 sc0 sc1
	s_waitcnt vmcnt(23)
	v_pk_add_f32 v[136:137], v[136:137], v[176:177]
	v_pk_add_f32 v[138:139], v[138:139], v[178:179]
	global_store_dwordx4 v58, v[136:139], s[10:11] offset:256 sc0 sc1
	s_waitcnt vmcnt(23)
	v_pk_add_f32 v[140:141], v[140:141], v[180:181]
	v_pk_add_f32 v[142:143], v[142:143], v[182:183]
	global_store_dwordx4 v59, v[140:143], s[10:11] offset:256 sc0 sc1
	s_waitcnt vmcnt(23)
	v_pk_add_f32 v[144:145], v[144:145], v[184:185]
	v_pk_add_f32 v[146:147], v[146:147], v[186:187]
	global_store_dwordx4 v56, v[144:147], s[10:11] offset:320 sc0 sc1
	s_waitcnt vmcnt(23)
	v_pk_add_f32 v[148:149], v[148:149], v[188:189]
	v_pk_add_f32 v[150:151], v[150:151], v[190:191]
	global_store_dwordx4 v57, v[148:151], s[10:11] offset:320 sc0 sc1
	s_waitcnt vmcnt(23)
	v_pk_add_f32 v[152:153], v[152:153], v[192:193]
	v_pk_add_f32 v[154:155], v[154:155], v[194:195]
	global_store_dwordx4 v58, v[152:155], s[10:11] offset:320 sc0 sc1
	s_waitcnt vmcnt(23)
	v_pk_add_f32 v[156:157], v[156:157], v[196:197]
	v_pk_add_f32 v[158:159], v[158:159], v[198:199]
	global_store_dwordx4 v59, v[156:159], s[10:11] offset:320 sc0 sc1
